# stack18_prio3
# speedup vs baseline: 1.0150x; 1.0150x over previous
.LBB3_8:
	s_setprio 0
	s_cmp_eq_u32 s90, 0
	s_cbranch_scc1 .Lrec2_p_a
	s_setprio 1

.LBB3_36:
	s_setprio 0
	s_cmp_lg_u32 s90, 0
	s_cbranch_scc1 .Lrec2_p_b
	s_setprio 1
